# layer-0 router bias moved from four converting workgroups (critical path) to four late-joining workgroups
# baseline (speedup 1.0000x reference)
; #define LAS __attribute__((address_space(3)))
; #define REP(k) _Pragma("unroll") for (int rep_ = 0; rep_ < 1 + (int)(((REP_MASK) >> (k)) & 1u); ++rep_)
; #define SEAM(k) do { if (IN(k) && IN((k) + 1)) xcd_barrier(bar); } while (0)
; __global__ void __launch_bounds__(512, 2) mk_fwd(Params p) {
;     ...
;     const int tid = threadIdx.x, G = gridDim.x, bx = blockIdx.x;
;     volatile LAS unsigned* misc = (volatile LAS unsigned*)(lds + MISC_OFF);
;     if (tid < 16) misc[tid] = 0u;
;     __syncthreads();
;     const int lo = p.ph_lo, hi = p.ph_hi;
;     XcdBarrier bar; bar.bar = (unsigned*)(p.ws + WS_CTL); bar.x = 0; bar.st = misc + 8; bar.gsz = (unsigned)G;
;     if (hi - lo > 1) bar = xcd_barrier_post((unsigned*)(p.ws + WS_CTL), misc + 8, (unsigned)G);
;     const bool split_ok = (G == 256) && (hi - lo > 1);
;     XcdBarrier bar2; bar2.bar = (unsigned*)(p.ws + WS_CTL) + 4096; bar2.x = 0; bar2.st = misc + 12; bar2.gsz = (unsigned)MIX_GW;
;     if (split_ok && bx < MIX_GW) bar2 = xcd_barrier_post((unsigned*)(p.ws + WS_CTL) + 4096, misc + 12, (unsigned)MIX_GW);
;     ...
;     if (IN(0)) { if (EN(0)) REP(0) ph_mod(p, lds); if (EN(1)) REP(1) ph_tables(p, lds); if (EN(2)) REP(2) { if (G == 256) { if (bx >= 192) ph_weights(p, lds, 0, 240, bx - 192, 64); } else ph_weights(p, lds, 0, 6880, bx, G); } }
;     SEAM(0);
;     for (int l = 0; l < 2; ++l) {
;         const int pb = 1 + 10 * l;
.LBB0_329:
	s_ashr_i32 s0, s2, 31
	v_writelane_b32 v249, s0, 51
	s_lshr_b32 s0, s0, 29
	s_add_i32 s0, s2, s0
	s_add_i32 s12, s2, 0x70
	s_and_b32 s1, s0, -8
	s_lshl_b32 s4, s12, 1
	s_sub_i32 s1, s2, s1
	s_add_i32 s5, s4, 0xffffe520
	s_cmpk_gt_u32 s2, 0xcff
	s_cselect_b32 s21, 16, 0
	s_cselect_b32 s18, 0x800, 0
	s_cselect_b32 s13, 0xd00, 0
	s_cselect_b32 s20, 0x8000, 0
	s_cmpk_lt_u32 s2, 0xd00
	s_cselect_b32 s31, s4, s5
	s_or_b32 s5, s4, 1
	s_addk_i32 s4, 0xe521
	s_lshl_b32 s6, s1, 5
	s_cmp_lt_i32 s1, 0
	s_mul_i32 s7, s1, 33
	s_cselect_b32 s22, 53, 52
	s_cselect_b32 s3, s7, s6
	s_cmpk_lt_u32 s2, 0xd00
	s_cselect_b32 s19, s5, s4
	s_cmpk_gt_u32 s2, 0xcff
	s_cselect_b32 s23, 0x200000, 0
	s_add_u32 s16, s26, 0x24400000
	s_addc_u32 s17, s27, 0
	s_cmpk_lg_i32 s58, 0x100
	s_cselect_b64 s[4:5], -1, 0
	s_cmp_gt_i32 s2, 3
	s_cselect_b64 s[6:7], -1, 0
	s_or_b64 s[4:5], s[6:7], s[4:5]
	v_writelane_b32 v249, s3, 52
	s_nor_b64 s[4:5], s[10:11], s[4:5]
	v_writelane_b32 v249, s4, 53
	s_mul_i32 s1, s22, s1
	s_mov_b32 s61, 0
	v_writelane_b32 v249, s5, 54
	s_add_u32 s4, s26, 0x3b380000
	s_addc_u32 s5, s27, 0
	s_add_u32 s7, s26, 0x32300000
	v_writelane_b32 v249, s4, 55
	s_addc_u32 s43, s27, 0
	v_mov_b32_e32 v1, 0x12e0
	v_writelane_b32 v249, s5, 56
	s_add_u32 s4, s26, 0x100000
	s_addc_u32 s5, s27, 0
	s_lshl_b32 s3, s2, 5
	s_add_u32 s62, s26, 0x37300000
	v_writelane_b32 v249, s4, 57
	s_addc_u32 s63, s27, 0
	s_mov_b64 s[52:53], s[72:73]
	v_writelane_b32 v249, s5, 58
	s_add_u32 s4, s26, 0x31220000
	v_writelane_b32 v249, s3, 59
	s_addc_u32 s5, s27, 0
	v_writelane_b32 v249, s4, 60
	v_mov_b32_e32 v195, 0
	v_mov_b32_e32 v217, 0x358637bd
	v_writelane_b32 v249, s5, 61
	s_add_u32 s4, s26, 0x20400000
	s_addc_u32 s5, s27, 0
	v_writelane_b32 v249, s4, 62
	v_mov_b32_e32 v219, 0x260
	v_mov_b32_e32 v221, 1
	v_writelane_b32 v249, s5, 63
	s_add_u32 s4, s26, 0x1c400000
	s_addc_u32 s5, s27, 0
	v_writelane_b32 v250, s4, 0
	v_readlane_b32 vcc_lo, v249, 47
	v_readlane_b32 vcc_hi, v249, 48
	v_writelane_b32 v250, s5, 1
	s_add_u32 s4, s70, 0x2000
	s_addc_u32 s5, s71, 0
	s_lshl_b32 s3, s58, 5
	s_add_u32 s54, s26, 0x1000
	v_writelane_b32 v250, s4, 2
	s_addc_u32 s55, s27, 0
	v_readlane_b32 s80, v249, 0
	v_writelane_b32 v250, s5, 3
	s_add_u32 s4, s26, 0x1100
	v_writelane_b32 v250, s3, 4
	s_addc_u32 s5, s27, 0
	v_writelane_b32 v250, s4, 5
	v_readlane_b32 s84, v249, 4
	v_readlane_b32 s85, v249, 5
	v_writelane_b32 v250, s5, 6
	s_add_u32 s4, s26, 0x1200
	s_addc_u32 s5, s27, 0
	v_writelane_b32 v250, s4, 7
	v_readlane_b32 s81, v249, 1
	v_readlane_b32 s82, v249, 2
	v_writelane_b32 v250, s5, 8
	s_add_u32 s4, s26, 0x1300
	s_addc_u32 s5, s27, 0
	v_writelane_b32 v250, s4, 9
	s_cmp_eq_u32 s96, 15
	v_readlane_b32 s83, v249, 3
	v_writelane_b32 v250, s5, 10
	s_cselect_b64 s[4:5], -1, 0
	v_writelane_b32 v250, s4, 11
	s_cmp_eq_u32 s96, 14
	v_readlane_b32 s64, v249, 29
	v_writelane_b32 v250, s5, 12
	s_cselect_b64 s[4:5], -1, 0
	v_writelane_b32 v250, s4, 13
	s_cmp_eq_u32 s96, 13
	v_readlane_b32 s74, v249, 39
	v_writelane_b32 v250, s5, 14
	s_cselect_b64 s[4:5], -1, 0
	v_writelane_b32 v250, s4, 15
	s_cmp_eq_u32 s96, 12
	v_readlane_b32 s75, v249, 40
	v_writelane_b32 v250, s5, 16
	s_cselect_b64 s[4:5], -1, 0
	v_writelane_b32 v250, s4, 17
	s_cmp_eq_u32 s96, 11
	v_readlane_b32 s72, v249, 37
	v_writelane_b32 v250, s5, 18
	s_cselect_b64 s[4:5], -1, 0
	v_writelane_b32 v250, s4, 19
	s_cmp_eq_u32 s96, 10
	v_readlane_b32 s73, v249, 38
	v_writelane_b32 v250, s5, 20
	s_cselect_b64 s[4:5], -1, 0
	v_writelane_b32 v250, s4, 21
	s_cmp_eq_u32 s96, 9
	v_readlane_b32 s79, v249, 44
	v_writelane_b32 v250, s5, 22
	s_cselect_b64 s[4:5], -1, 0
	v_writelane_b32 v250, s4, 23
	s_cmp_eq_u32 s96, 8
	v_readlane_b32 s70, v249, 35
	v_writelane_b32 v250, s5, 24
	s_cselect_b64 s[4:5], -1, 0
	v_writelane_b32 v250, s4, 25
	s_cmp_eq_u32 s96, 7
	v_readlane_b32 s71, v249, 36
	v_writelane_b32 v250, s5, 26
	s_cselect_b64 s[4:5], -1, 0
	v_writelane_b32 v250, s4, 27
	s_cmp_eq_u32 s96, 6
	v_readlane_b32 s76, v249, 41
	v_writelane_b32 v250, s5, 28
	s_cselect_b64 s[4:5], -1, 0
	v_writelane_b32 v250, s4, 29
	s_cmp_eq_u32 s96, 5
	v_readlane_b32 s77, v249, 42
	v_writelane_b32 v250, s5, 30
	s_cselect_b64 s[4:5], -1, 0
	v_writelane_b32 v250, s4, 31
	s_cmp_eq_u32 s96, 4
	v_readlane_b32 s65, v249, 30
	v_writelane_b32 v250, s5, 32
	s_cselect_b64 s[4:5], -1, 0
	v_writelane_b32 v250, s4, 33
	s_cmp_eq_u32 s96, 3
	v_readlane_b32 s69, v249, 34
	v_writelane_b32 v250, s5, 34
	s_cselect_b64 s[4:5], -1, 0
	v_writelane_b32 v250, s4, 35
	s_cmp_eq_u32 s96, 2
	v_readlane_b32 s78, v249, 43
	v_writelane_b32 v250, s5, 36
	s_cselect_b64 s[4:5], -1, 0
	v_writelane_b32 v250, s4, 37
	s_cmp_eq_u32 s96, 1
	v_readlane_b32 s68, v249, 33
	v_writelane_b32 v250, s5, 38
	s_cselect_b64 s[4:5], -1, 0
	v_writelane_b32 v250, s4, 39
	s_cmp_eq_u32 s96, 0
	v_readlane_b32 s66, v249, 31
	v_writelane_b32 v250, s5, 40
	s_cselect_b64 s[4:5], -1, 0
	v_writelane_b32 v250, s4, 41
	v_readlane_b32 s67, v249, 32
	v_readlane_b32 s86, v249, 6
	v_writelane_b32 v250, s5, 42
	s_lshl_b32 s4, s96, 8
	s_add_u32 s4, s26, s4
	s_addc_u32 s5, s27, 0
	s_add_u32 s10, s4, 0x1400
	s_addc_u32 s11, s5, 0
	v_writelane_b32 v250, s10, 43
	s_add_u32 s4, s4, 0x2400
	s_addc_u32 s5, s5, 0
	v_writelane_b32 v250, s11, 44
	v_writelane_b32 v250, s4, 45
	v_readlane_b32 s87, v249, 7
	v_mov_b32_e32 v248, -1
	v_writelane_b32 v250, s5, 46
	s_add_u32 s4, s26, 0x3400
	s_addc_u32 s5, s27, 0
	s_add_u32 s14, s26, 0x1200000
	s_addc_u32 s15, s27, 0
	s_add_u32 s38, s26, 0x2c00000
	v_writelane_b32 v250, s4, 47
	s_addc_u32 s39, s27, 0
	v_mov_b32_e32 v218, 0xf149f2ca
	v_writelane_b32 v250, s5, 48
	s_add_u32 s4, s26, 0x26400000
	s_addc_u32 s5, s27, 0
; __device__ __forceinline__ void xcd_barrier_complete(unsigned* bar, unsigned x, unsigned& nloc, unsigned& nx, const unsigned G) {
;     unsigned sum, cnt, mine, sp = 0u;
;     for (;;) {
;         sum = 0u; cnt = 0u; mine = 0u;
; #pragma unroll
;         for (unsigned j = 0; j < 16; ++j) { const unsigned c = xb_ld(&bar[XB_XCNT(j)]); sum += c; cnt += (c > 0u) ? 1u : 0u; mine = (j == x) ? c : mine; }
;         if (sum == G) break;
;         __builtin_amdgcn_s_sleep(1);
; __global__ void __launch_bounds__(512, 2) mk_fwd(Params p) {
;     ...
;     const int lo = p.ph_lo, hi = p.ph_hi;
;     XcdBarrier bar; bar.bar = (unsigned*)(p.ws + WS_CTL); bar.x = 0; bar.st = misc + 8; bar.gsz = (unsigned)G;
;     if (hi - lo > 1) bar = xcd_barrier_post((unsigned*)(p.ws + WS_CTL), misc + 8, (unsigned)G);
;     const bool split_ok = (G == 256) && (hi - lo > 1);
;     XcdBarrier bar2; bar2.bar = (unsigned*)(p.ws + WS_CTL) + 4096; bar2.x = 0; bar2.st = misc + 12; bar2.gsz = (unsigned)MIX_GW;
;     if (split_ok && bx < MIX_GW) bar2 = xcd_barrier_post((unsigned*)(p.ws + WS_CTL) + 4096, misc + 12, (unsigned)MIX_GW);
;     ...
;     if (IN(0)) { if (EN(0)) REP(0) ph_mod(p, lds); if (EN(1)) REP(1) ph_tables(p, lds); if (EN(2)) REP(2) { if (G == 256) { if (bx >= 192) ph_weights(p, lds, 0, 240, bx - 192, 64); } else ph_weights(p, lds, 0, 6880, bx, G); } }
;     SEAM(0);
;     for (int l = 0; l < 2; ++l) {
;         const int pb = 1 + 10 * l;
;         const char* H = (const char*)(p.ws + WS_H);
;         if (EN(3) && IN(pb + 0)) REP(3) { if (G == 256 && !split_ok && bx < 4) ph_rbias(p, l, bx); if (l == 0) ph_norm1_l0(p); else ph_norm1(p, 1, lds); }
;         SEAM(pb + 0);
;         const bool split = split_ok && l == 0 && EN(2);
;         const int vG = split ? MIX_GW : G;
;         if (EN(4) && IN(pb + 1) && (!split || bx < MIX_GW)) REP(4) {
;             SchedProj S{H, (const char*)(p.ws + WS_WIN) + (size_t)l * NPROJ * 2048 * 2, (const char*)(p.ws + WS_WPQ) + (size_t)l * 512 * 2048 * 2, vG, bx};
;             EpiProj E{(bf16_t*)(p.ws + WS_PROJ), (bf16_t*)(p.ws + WS_PQT), (const float*)(p.ws + WS_ROPE), (const float*)(p.ws + WS_ROPE) + NT * 8};
;             pg8::gemm_phase<EpiProj, SchedProj>(lds, 2048, 2048, 2048, S, E);
;         }
;         if (split) { if (bx < MIX_GW && IN(pb + 1) && IN(pb + 2)) xcd_barrier(bar2); } else SEAM(pb + 1);
	v_writelane_b32 v250, s4, 49
	s_add_u32 s3, s26, 0x29800000
	v_mov_b32_e32 v227, 0x7f800000
	v_writelane_b32 v250, s5, 50
	v_writelane_b32 v250, s3, 51
	s_addc_u32 s3, s27, 0
	s_add_u32 s4, s26, 0x180000
	s_addc_u32 s5, s27, 0
	v_writelane_b32 v250, s4, 52
	s_nop 1
	v_writelane_b32 v250, s5, 53
	s_add_u32 s4, s26, 0x1c0000
	s_addc_u32 s5, s27, 0
	v_writelane_b32 v250, s4, 54
	s_cmpk_lt_i32 s2, 0x1e0
	s_nop 0
	v_writelane_b32 v250, s5, 55
	s_cselect_b64 s[4:5], -1, 0
	v_writelane_b32 v250, s4, 56
	s_nop 1
	v_writelane_b32 v250, s5, 57
	s_add_i32 s5, s2, 0x60
	s_lshl_b32 s4, s2, 3
	s_lshr_b32 s10, s5, 3
	s_and_b32 s4, s4, 56
	s_and_b32 s10, s10, 30
	s_add_i32 s10, s10, s4
	s_bfe_u32 s5, s5, 0x10003
	s_lshr_b32 s4, s10, 1
	v_writelane_b32 v250, s5, 58
	s_or_b32 s2, s4, 64
	v_writelane_b32 v250, s2, 59
	s_lshl_b32 s4, s10, 19
	s_lshl_b32 s2, s5, 20
	v_writelane_b32 v250, s2, 61
	s_add_u32 s2, s16, s4
	v_writelane_b32 v250, s2, 62
	s_addc_u32 s2, s17, 0
	s_ashr_i32 s42, s0, 3
	s_add_i32 s1, s1, s42
	s_mul_hi_i32 s0, s1, 0x4ec4ec4f
	s_lshr_b32 s4, s0, 31
	s_ashr_i32 s0, s0, 5
	s_add_i32 s0, s0, s4
	s_mul_i32 s4, s0, 0x68
	s_sub_i32 s1, s1, s4
	s_bfe_i32 s4, s1, 0x80000
	s_bfe_u32 s4, s4, 0x3000c
	s_add_i32 s4, s1, s4
	s_and_b32 s5, s4, 0xf8
	s_sub_i32 s1, s1, s5
	s_lshl_b32 s0, s0, 3
	s_bfe_i32 s4, s4, 0x80000
	s_sext_i32_i8 s1, s1
	s_sext_i32_i16 s10, s4
	s_add_i32 s4, s0, s1
	s_ashr_i32 s5, s4, 31
	s_ashr_i32 s0, s10, 3
	s_lshr_b32 s10, s10, 3
	s_lshl_b64 s[34:35], s[4:5], 20
	v_writelane_b32 v251, s0, 0
	s_add_u32 s0, s16, s34
	v_writelane_b32 v251, s0, 2
	s_addc_u32 s0, s17, s35
	s_bfe_i64 s[10:11], s[10:11], 0x100000
	v_writelane_b32 v251, s0, 3
	s_lshl_b64 s[0:1], s[10:11], 20
	v_writelane_b32 v251, s0, 4
	v_writelane_b32 v250, s2, 63
	s_nop 0
	v_writelane_b32 v251, s1, 5
	v_readlane_b32 s0, v249, 8
	v_readlane_b32 s1, v249, 9
	s_cmp_lt_i32 s0, 4
	s_cselect_b64 s[10:11], -1, 0
	s_cmp_gt_i32 s1, 3
	s_cselect_b64 s[34:35], -1, 0
	s_and_b64 s[10:11], s[10:11], s[34:35]
	s_and_b64 s[0:1], vcc, s[10:11]
	v_writelane_b32 v251, s0, 6
	s_nop 1
	v_writelane_b32 v251, s1, 7
	s_add_u32 s0, s26, 0x4200
	s_addc_u32 s1, s27, 0
	v_writelane_b32 v251, s0, 8
	s_nop 1
	v_writelane_b32 v251, s1, 9
	s_add_u32 s0, s26, 0x4400
	s_addc_u32 s1, s27, 0
	v_writelane_b32 v251, s0, 10
	s_nop 1
	v_writelane_b32 v251, s1, 11
	s_add_u32 s0, s26, 0x4500
	s_addc_u32 s1, s27, 0
	v_writelane_b32 v251, s0, 12
	s_nop 1
	v_writelane_b32 v251, s1, 13
	s_add_u32 s0, s26, 0x4600
	s_addc_u32 s1, s27, 0
	v_writelane_b32 v251, s0, 14
	s_nop 1
	v_writelane_b32 v251, s1, 15
	s_add_u32 s0, s26, 0x4700
	s_addc_u32 s1, s27, 0
	v_writelane_b32 v251, s0, 16
	s_nop 1
	v_writelane_b32 v251, s1, 17
	s_add_u32 s0, s26, 0x4800
	s_addc_u32 s1, s27, 0
	v_writelane_b32 v251, s0, 18
	s_nop 1
	v_writelane_b32 v251, s1, 19
	s_add_u32 s0, s26, 0x4900
	s_addc_u32 s1, s27, 0
	v_writelane_b32 v251, s0, 20
	s_nop 1
	v_writelane_b32 v251, s1, 21
	s_add_u32 s0, s26, 0x4a00
	s_addc_u32 s1, s27, 0
	v_writelane_b32 v251, s0, 22
	s_nop 1
	v_writelane_b32 v251, s1, 23
	s_add_u32 s0, s26, 0x4b00
	s_addc_u32 s1, s27, 0
	v_writelane_b32 v251, s0, 24
	s_nop 1
	v_writelane_b32 v251, s1, 25
	s_add_u32 s0, s26, 0x4c00
	s_addc_u32 s1, s27, 0
	v_writelane_b32 v251, s0, 26
	s_nop 1
	v_writelane_b32 v251, s1, 27
	s_add_u32 s0, s26, 0x4d00
	s_addc_u32 s1, s27, 0
	v_writelane_b32 v251, s0, 28
	s_nop 1
	v_writelane_b32 v251, s1, 29
	s_add_u32 s0, s26, 0x4e00
	s_addc_u32 s1, s27, 0
	v_writelane_b32 v251, s0, 30
	s_nop 1
	v_writelane_b32 v251, s1, 31
	s_add_u32 s0, s26, 0x4f00
	s_addc_u32 s1, s27, 0
	v_writelane_b32 v251, s0, 32
	s_nop 1
	v_writelane_b32 v251, s1, 33
	s_add_u32 s0, s26, 0x5000
	s_addc_u32 s1, s27, 0
	v_writelane_b32 v251, s0, 34
	s_nop 1
	v_writelane_b32 v251, s1, 35
	s_add_u32 s0, s26, 0x5100
	s_addc_u32 s1, s27, 0
	v_writelane_b32 v251, s0, 36
	s_nop 1
	v_writelane_b32 v251, s1, 37
	s_add_u32 s0, s26, 0x5200
	s_addc_u32 s1, s27, 0
	v_writelane_b32 v251, s0, 38
	s_nop 1
	v_writelane_b32 v251, s1, 39
	s_add_u32 s0, s26, 0x5300
	s_addc_u32 s1, s27, 0
	v_writelane_b32 v251, s0, 40
	s_cmp_eq_u32 s97, 15
	s_nop 0
	v_writelane_b32 v251, s1, 41
	s_cselect_b64 s[0:1], -1, 0
	v_writelane_b32 v251, s0, 42
	s_cmp_eq_u32 s97, 14
	s_nop 0
	v_writelane_b32 v251, s1, 43
	s_cselect_b64 s[0:1], -1, 0
	v_writelane_b32 v251, s0, 44
	s_cmp_eq_u32 s97, 13
	s_nop 0
	v_writelane_b32 v251, s1, 45
	s_cselect_b64 s[0:1], -1, 0
	v_writelane_b32 v251, s0, 46
	s_cmp_eq_u32 s97, 12
	s_nop 0
	v_writelane_b32 v251, s1, 47
	s_cselect_b64 s[0:1], -1, 0
	v_writelane_b32 v251, s0, 48
	s_cmp_eq_u32 s97, 11
	s_nop 0
	v_writelane_b32 v251, s1, 49
	s_cselect_b64 s[0:1], -1, 0
	v_writelane_b32 v251, s0, 50
	s_cmp_eq_u32 s97, 10
	s_nop 0
	v_writelane_b32 v251, s1, 51
	s_cselect_b64 s[0:1], -1, 0
	v_writelane_b32 v251, s0, 52
	s_cmp_eq_u32 s97, 9
	s_nop 0
	v_writelane_b32 v251, s1, 53
	s_cselect_b64 s[0:1], -1, 0
	v_writelane_b32 v251, s0, 54
	s_cmp_eq_u32 s97, 8
	s_nop 0
	v_writelane_b32 v251, s1, 55
	s_cselect_b64 s[0:1], -1, 0
	v_writelane_b32 v251, s0, 56
	s_cmp_eq_u32 s97, 7
	s_nop 0
	v_writelane_b32 v251, s1, 57
	s_cselect_b64 s[0:1], -1, 0
	v_writelane_b32 v251, s0, 58
	s_cmp_eq_u32 s97, 6
	s_nop 0
	v_writelane_b32 v251, s1, 59
	s_cselect_b64 s[0:1], -1, 0
	v_writelane_b32 v251, s0, 60
	s_cmp_eq_u32 s97, 5
	s_nop 0
	v_writelane_b32 v251, s1, 61
	s_cselect_b64 s[0:1], -1, 0
	v_writelane_b32 v251, s0, 62
	s_cmp_eq_u32 s97, 4
	s_nop 0
	v_writelane_b32 v251, s1, 63
	s_cselect_b64 s[0:1], -1, 0
	v_writelane_b32 v252, s0, 0
	s_cmp_eq_u32 s97, 3
	s_nop 0
	v_writelane_b32 v252, s1, 1
	s_cselect_b64 s[0:1], -1, 0
	v_writelane_b32 v252, s0, 2
; __device__ __forceinline__ int opaque_tid() { int t = threadIdx.x; asm volatile("" : "+v"(t)); return t; }
; #define REP(k) _Pragma("unroll") for (int rep_ = 0; rep_ < 1 + (int)(((REP_MASK) >> (k)) & 1u); ++rep_)
; __device__ __forceinline__ void ph_rbias(const Params& p, const int l, const int b) {
;     const int tid = opaque_tid(), e = tid >> 5, part = tid & 31;
;     const float* sh = (const float*)(p.ws + WS_MOD) + ((size_t)l * 4 + b) * 12288 + 3 * 2048 + part * 64;
;     const bf16_t* w = (const bf16_t*)(p.ws + WS_WRT) + ((size_t)l * 16 + e) * 2048 + part * 64;
; __global__ void __launch_bounds__(512, 2) mk_fwd(Params p) {
;     ...
;         if (IN(pb + 2)) {
;             if (!split || bx < MIX_GW) {
;                 if (EN(5)) REP(5) ph_fft(p, lds, bx, vG);
;                 __syncthreads();
;                 if (EN(8)) REP(8) ph_mixers(p, l, lds, bx, vG);
;             } else { if (bx - MIX_GW < 4) ph_rbias(p, 0, bx - MIX_GW); ph_weights(p, lds, 240, 6880, bx - MIX_GW, G - MIX_GW); }
	s_cmp_eq_u32 s97, 2
	s_nop 0
	v_writelane_b32 v252, s1, 3
	s_cselect_b64 s[0:1], -1, 0
	v_writelane_b32 v252, s0, 4
	s_cmp_eq_u32 s97, 1
	s_nop 0
	v_writelane_b32 v252, s1, 5
	s_cselect_b64 s[0:1], -1, 0
	v_writelane_b32 v252, s0, 6
	s_cmp_eq_u32 s97, 0
	s_nop 0
	v_writelane_b32 v252, s1, 7
	s_cselect_b64 s[0:1], -1, 0
	v_writelane_b32 v252, s0, 8
	s_nop 1
	v_writelane_b32 v252, s1, 9
	s_lshl_b32 s0, s97, 8
	s_add_u32 s0, s8, s0
	s_addc_u32 s1, s9, 0
	s_add_u32 s8, s0, 0x1400
	s_addc_u32 s9, s1, 0
	v_writelane_b32 v252, s8, 10
	s_add_u32 s0, s0, 0x2400
	s_addc_u32 s1, s1, 0
	v_writelane_b32 v252, s9, 11
	v_writelane_b32 v252, s0, 12
	s_nop 1
	v_writelane_b32 v252, s1, 13
	s_add_u32 s0, s26, 0x7400
	s_addc_u32 s1, s27, 0
	v_writelane_b32 v252, s0, 14
	s_nop 1
	v_writelane_b32 v252, s1, 15
	v_readlane_b32 s0, v249, 28
	s_cmpk_lt_u32 s0, 0x84
	s_cselect_b64 s[0:1], -1, 0
	v_writelane_b32 v252, s0, 16
	s_nop 1
	v_writelane_b32 v252, s1, 17
	v_readlane_b32 s0, v249, 28
	s_add_i32 s60, s0, 0xffffff80
	s_mul_i32 s0, s60, 0xc000
	s_add_u32 s0, s26, s0
	s_mul_hi_u32 s1, s60, 0xc000
	s_addc_u32 s1, s27, s1
	s_add_u32 s0, s0, 0x106000
	s_addc_u32 s1, s1, 0
	v_writelane_b32 v252, s0, 18
	s_lshl_b64 s[8:9], s[60:61], 6
	s_nop 0
	v_writelane_b32 v252, s1, 19
	s_add_u32 s0, s7, s8
	s_addc_u32 s1, s43, s9
	v_writelane_b32 v252, s0, 20
	s_add_i32 s30, s58, 0xffffff80
	s_nop 0
	v_writelane_b32 v252, s1, 21
	v_readlane_b32 s0, v249, 28
	s_cmpk_lt_u32 s0, 0x1a70
	s_cselect_b64 s[0:1], -1, 0
	v_writelane_b32 v252, s0, 22
	s_cmpk_gt_u32 s31, 0x1df
	s_cselect_b64 s[8:9], -1, 0
	v_writelane_b32 v252, s1, 23
	s_waitcnt vmcnt(15)
	v_sub_co_u32_e64 v2, s[0:1], s31, v1
	s_nop 1
	v_writelane_b32 v252, s0, 24
	s_nop 1
	v_writelane_b32 v252, s1, 25
	v_readfirstlane_b32 s0, v2
	v_mov_b32_e32 v2, 0x2e0
	v_writelane_b32 v252, s8, 26
	v_sub_co_u32_e64 v3, s[34:35], s31, v2
	s_nop 0
	v_writelane_b32 v252, s9, 27
	s_lshr_b32 s1, s0, 7
	s_xor_b64 s[8:9], s[34:35], -1
	s_add_i32 s60, s21, s1
	v_writelane_b32 v252, s8, 28
	s_lshl_b32 s0, s0, 3
	s_and_b32 s0, s0, 0x380
	v_writelane_b32 v252, s9, 29
	s_lshl_b64 s[8:9], s[60:61], 23
	s_add_u32 s1, s84, s8
	s_addc_u32 s5, s85, s9
	s_lshl_b32 s8, s0, 13
	s_add_u32 s1, s1, s8
	s_addc_u32 s8, s5, 0
	s_lshl_b32 s5, s31, 7
	s_and_b32 s10, s5, 0x700
	s_lshl_b32 s11, s10, 2
	s_add_u32 s1, s1, s11
	v_writelane_b32 v252, s1, 30
	s_addc_u32 s1, s8, 0
	s_add_u32 s2, s26, 0x14400000
	s_addc_u32 s44, s27, 0
	s_lshl_b64 s[8:9], s[60:61], 22
	v_writelane_b32 v252, s1, 31
	s_add_u32 s1, s2, s8
	s_addc_u32 s8, s44, s9
	s_lshl_b32 s9, s10, 11
	s_add_u32 s1, s1, s9
	s_addc_u32 s8, s8, 0
	s_lshl_b32 s0, s0, 1
	s_add_u32 s0, s1, s0
	v_writelane_b32 v252, s0, 33
	s_addc_u32 s0, s8, 0
	v_writelane_b32 v252, s0, 35
	v_readfirstlane_b32 s0, v3
	s_and_b32 s1, s31, 6
	s_cmpk_lt_u32 s0, 0x800
	s_cselect_b32 s8, s81, s83
	s_cselect_b32 s9, s80, s82
	s_lshl_b32 s28, s0, 4
	s_and_b32 s29, s28, 0x7800
	s_or_b32 s29, s20, s29
	s_and_b32 s28, s28, 0x780
	s_or_b32 s34, s29, s28
	s_lshl_b32 s34, s34, 12
	s_add_u32 s9, s9, s34
	s_addc_u32 s8, s8, 0
	s_lshl_b32 s34, s1, 9
	s_add_u32 s5, s9, s34
	v_writelane_b32 v252, s5, 37
	s_addc_u32 s5, s8, 0
	s_add_u32 s96, s26, 0x4400000
	s_addc_u32 s97, s27, 0
	s_lshr_b32 s0, s0, 4
	s_lshl_b32 s1, s1, 8
	s_and_b32 s0, s0, 0xfffff80
	s_add_i32 s0, s0, s1
	s_add_i32 s60, s29, s0
	s_lshl_b64 s[8:9], s[60:61], 12
	s_add_u32 s0, s96, s8
	s_addc_u32 s1, s97, s9
	s_lshl_b32 s8, s28, 1
	v_writelane_b32 v252, s5, 38
	s_add_u32 s0, s0, s8
	v_writelane_b32 v252, s0, 39
	s_addc_u32 s0, s1, 0
	v_writelane_b32 v252, s0, 40
	s_lshl_b32 s0, s31, 3
	s_and_b32 s0, s0, 0x1f80
	s_add_i32 s60, s0, 0xfffff100
	s_add_i32 s8, s18, s60
	s_mov_b32 s9, s61
	s_lshl_b64 s[8:9], s[8:9], 13
	s_add_u32 s0, s74, s8
	s_addc_u32 s1, s75, s9
	s_add_u32 s0, s0, s11
	s_addc_u32 s1, s1, 0
	v_writelane_b32 v252, s0, 41
	s_nop 1
	v_writelane_b32 v252, s1, 42
	s_lshl_b32 s0, s18, 2
	s_add_u32 s0, s72, s0
	s_addc_u32 s1, s73, 0
	s_lshl_b64 s[8:9], s[60:61], 2
	s_add_u32 s0, s0, s8
	s_addc_u32 s1, s1, s9
	v_writelane_b32 v252, s0, 43
	s_add_u32 s92, s26, 0x3400000
	s_addc_u32 s93, s27, 0
	v_writelane_b32 v252, s1, 44
	s_or_b32 s0, s18, s10
	s_lshl_b32 s0, s0, 12
	s_add_u32 s0, s92, s0
	s_addc_u32 s1, s93, 0
	s_lshl_b64 s[8:9], s[60:61], 1
	s_add_u32 s0, s0, s8
	s_addc_u32 s1, s1, s9
	v_writelane_b32 v252, s0, 45
	s_nop 1
	v_writelane_b32 v252, s1, 46
	s_mul_i32 s0, s31, 0x8889
	s_lshr_b32 s1, s0, 20
	s_lshr_b32 s0, s0, 13
	s_and_b32 s34, s0, 0xff80
	s_mul_i32 s1, s1, 30
	s_add_i32 s0, s18, s34
	s_sub_i32 s1, s31, s1
	s_mulk_i32 s0, 0x3c00
	s_add_u32 s0, s52, s0
	s_addc_u32 s8, s53, 0
	s_lshl_b32 s9, s1, 7
	s_and_b32 s64, s9, 0xff80
	s_lshl_b32 s9, s64, 2
	s_add_u32 s10, s0, s9
	s_addc_u32 s11, s8, 0
	v_writelane_b32 v252, s10, 47
	s_and_b32 s0, s1, 0xffff
	s_nop 0
	v_writelane_b32 v252, s11, 48
	v_writelane_b32 v252, s0, 49
	s_add_i32 s0, s64, 0xfffffe00
	s_add_u32 s5, s0, s13
	s_addc_u32 s22, 0, 0
	s_add_u32 s23, s38, s23
	s_addc_u32 s59, s39, 0
	v_sub_co_u32_e64 v3, s[0:1], s19, v1
	s_cmpk_gt_u32 s19, 0x1df
	s_nop 0
	v_writelane_b32 v252, s0, 50
	s_cselect_b64 s[8:9], -1, 0
	s_nop 0
	v_writelane_b32 v252, s1, 51
	v_readfirstlane_b32 s0, v3
	v_writelane_b32 v252, s8, 52
	v_sub_co_u32_e64 v3, s[36:37], s19, v2
	s_nop 0
	v_writelane_b32 v252, s9, 53
	s_lshr_b32 s1, s0, 7
	s_xor_b64 s[8:9], s[36:37], -1
	s_add_i32 s60, s21, s1
	v_writelane_b32 v252, s8, 54
	s_lshl_b32 s0, s0, 3
	s_and_b32 s0, s0, 0x380
	v_writelane_b32 v252, s9, 55
	s_lshl_b64 s[8:9], s[60:61], 23
	s_add_u32 s1, s84, s8
	s_addc_u32 s8, s85, s9
	s_lshl_b32 s9, s0, 13
	s_add_u32 s1, s1, s9
	s_addc_u32 s8, s8, 0
;     __device__ __forceinline__ bool next(int i, GUnit& u) const {
;         const int L = i * G + c; if (L >= 480) return false;
;         if (L < 416) { int pm, pn; pg8::dense_map(L, 32, 13, pm, pn); u.pm = pm; u.pn = pn; u.z = 0; u.a = H + (size_t)pm * 256 * 2048 * 2; u.b = WIN + (size_t)pn * 256 * 2048 * 2; }
;         else { int pm, pn; pg8::dense_map(L - 416, 2, 32, pm, pn); u.pm = pm; u.pn = pn + 64; u.z = 0; u.a = WPQ + (size_t)pm * 256 * 2048 * 2; u.b = H + (size_t)pn * 256 * 2048 * 2; }
; __device__ __forceinline__ bool tdecode(const Params& p, int it, TDesc& d) {
;     if (it >= 2 * 6880) return false;
;     const int l = it / 6880; int r = it % 6880;
;     d.ksc = nullptr;
;     if (r < 480) { const int kt = r / 30, nt = r % 30;
;         d.src = p.in[6] + ((size_t)l * 2048 + kt * 128) * DIN + nt * 128; d.lds_ = DIN;
;         d.dst = (nt < 4 ? (bf16_t*)(p.ws + WS_WPQ) + ((size_t)l * 512 + nt * 128) * 2048 : (bf16_t*)(p.ws + WS_WIN) + ((size_t)l * NPROJ + (nt - 4) * 128) * 2048) + kt * 128; d.ldd = 2048; return true; }
	s_lshl_b32 s9, s19, 7
	s_and_b32 s10, s9, 0x780
	s_lshl_b32 s11, s10, 2
	s_add_u32 s79, s1, s11
	s_addc_u32 s35, s8, 0
	s_lshl_b64 s[8:9], s[60:61], 22
	s_add_u32 s1, s2, s8
	s_addc_u32 s8, s44, s9
	s_lshl_b32 s9, s10, 11
	s_add_u32 s1, s1, s9
	s_addc_u32 s8, s8, 0
	s_lshl_b32 s0, s0, 1
	s_add_u32 s0, s1, s0
	v_writelane_b32 v252, s0, 56
	s_addc_u32 s0, s8, 0
	v_writelane_b32 v252, s0, 57
	v_readfirstlane_b32 s0, v3
	s_and_b32 s1, s19, 7
	s_cmpk_lt_u32 s0, 0x800
	s_cselect_b32 s8, s81, s83
	s_cselect_b32 s9, s80, s82
	s_lshl_b32 s21, s0, 4
	s_and_b32 s28, s21, 0x7800
	s_or_b32 s20, s20, s28
	s_and_b32 s21, s21, 0x780
	s_or_b32 s28, s20, s21
	s_lshl_b32 s28, s28, 12
	s_add_u32 s9, s9, s28
	s_addc_u32 s8, s8, 0
	s_lshl_b32 s28, s1, 9
	s_add_u32 s6, s9, s28
	s_addc_u32 s70, s8, 0
	s_lshr_b32 s0, s0, 4
	s_lshl_b32 s1, s1, 8
	s_and_b32 s0, s0, 0xfffff80
	s_add_i32 s0, s0, s1
	s_add_i32 s60, s20, s0
	s_lshl_b64 s[8:9], s[60:61], 12
	s_add_u32 s0, s96, s8
	s_addc_u32 s1, s97, s9
	s_lshl_b32 s8, s21, 1
	s_add_u32 s71, s0, s8
	s_addc_u32 s76, s1, 0
	s_lshl_b32 s0, s19, 3
	s_and_b32 s0, s0, 0x1f80
	s_add_i32 s60, s0, 0xfffff100
	s_add_i32 s8, s18, s60
	s_mov_b32 s9, s61
	s_lshl_b64 s[8:9], s[8:9], 13
	s_add_u32 s0, s74, s8
	s_addc_u32 s1, s75, s9
	s_add_u32 s0, s0, s11
	v_writelane_b32 v252, s6, 58
	s_addc_u32 s1, s1, 0
	v_writelane_b32 v252, s0, 60
	s_nop 1
	v_writelane_b32 v252, s1, 61
	s_or_b32 s0, s18, s10
	s_lshl_b32 s0, s0, 12
	s_add_u32 s0, s92, s0
	s_addc_u32 s1, s93, 0
	s_lshl_b64 s[8:9], s[60:61], 1
	s_add_u32 s0, s0, s8
	s_addc_u32 s1, s1, s9
	v_writelane_b32 v252, s0, 62
	s_nop 1
	v_writelane_b32 v252, s1, 63
	s_mul_i32 s0, s19, 0x8889
	s_lshr_b32 s1, s0, 20
	s_lshr_b32 s0, s0, 13
	s_and_b32 s77, s0, 0xff80
	s_mul_i32 s1, s1, 30
	s_add_i32 s0, s18, s77
	s_sub_i32 s1, s19, s1
	s_mulk_i32 s0, 0x3c00
	s_add_u32 s0, s52, s0
	s_addc_u32 s8, s53, 0
	s_lshl_b32 s9, s1, 7
	s_and_b32 s65, s9, 0xff80
	s_lshl_b32 s9, s65, 2
	s_add_u32 s10, s0, s9
	s_addc_u32 s11, s8, 0
	s_and_b32 s69, s1, 0xffff
	s_add_i32 s0, s65, 0xfffffe00
	s_add_u32 s78, s0, s13
	s_addc_u32 s68, 0, 0
	s_add_i32 s0, s30, s12
	v_writelane_b32 v253, s10, 0
	s_cmpk_lt_u32 s0, 0x1ae0
	s_cselect_b64 s[8:9], -1, 0
	v_writelane_b32 v253, s11, 1
	s_lshl_b32 s1, s0, 1
	v_writelane_b32 v253, s8, 2
	s_cmpk_gt_u32 s0, 0xd6f
	s_nop 0
	v_writelane_b32 v253, s9, 3
	s_cselect_b64 s[8:9], -1, 0
	s_add_i32 s10, s1, 0xffffe520
	s_or_b32 s11, s1, 1
	s_add_i32 s12, s1, 0xffffe521
	s_cmpk_lt_u32 s0, 0xd70
	s_cselect_b32 s0, s1, s10
	s_cselect_b32 s18, s11, s12
	s_cmpk_gt_i32 s0, 0x1df
	s_cselect_b64 s[10:11], -1, 0
	v_sub_co_u32_e64 v3, s[36:37], s0, v2
	v_writelane_b32 v253, s10, 4
	v_sub_co_u32_e64 v4, s[66:67], s0, v1
	s_nop 0
	v_writelane_b32 v253, s11, 5
	s_xor_b64 s[10:11], s[36:37], -1
	v_readfirstlane_b32 s1, v4
	v_writelane_b32 v253, s10, 6
	s_lshr_b32 s12, s1, 7
	s_nop 0
	v_writelane_b32 v253, s11, 7
	s_and_b64 s[10:11], s[8:9], exec
	s_cselect_b32 s19, 16, 0
	s_add_i32 s60, s19, s12
	s_lshl_b32 s1, s1, 3
	s_and_b32 s1, s1, 0x380
	s_lshl_b64 s[10:11], s[60:61], 23
	s_add_u32 s10, s84, s10
	s_addc_u32 s11, s85, s11
	s_lshl_b32 s12, s1, 13
	s_add_u32 s10, s10, s12
	s_addc_u32 s11, s11, 0
	s_lshl_b32 s12, s0, 7
	s_and_b32 s12, s12, 0x700
	s_lshl_b32 s13, s12, 2
	s_add_u32 s86, s10, s13
	s_addc_u32 s87, s11, 0
	s_lshl_b64 s[10:11], s[60:61], 22
	s_add_u32 s10, s2, s10
	s_addc_u32 s11, s44, s11
	s_lshl_b32 s20, s12, 11
	s_add_u32 s10, s10, s20
	s_addc_u32 s11, s11, 0
	s_lshl_b32 s1, s1, 1
	s_add_u32 s6, s10, s1
	s_addc_u32 s36, s11, 0
	s_and_b32 s1, s0, 6
	v_readfirstlane_b32 s20, v3
	s_cmpk_lt_u32 s20, 0x800
	s_cselect_b32 s21, s81, s83
	s_cselect_b32 s28, s80, s82
	s_lshl_b32 s29, s20, 4
	s_and_b32 s31, s29, 0x7800
	s_and_b64 s[10:11], s[8:9], exec
	s_cselect_b32 s33, 0x8000, 0
	s_or_b32 s10, s33, s31
	s_and_b32 s29, s29, 0x780
	s_or_b32 s11, s10, s29
	s_lshl_b32 s11, s11, 12
	s_add_u32 s11, s28, s11
	s_addc_u32 s21, s21, 0
	s_lshl_b32 s28, s1, 9
	s_add_u32 s37, s11, s28
	s_addc_u32 s57, s21, 0
	s_lshr_b32 s11, s20, 4
	s_lshl_b32 s1, s1, 8
	s_and_b32 s11, s11, 0xfffff80
	s_add_i32 s11, s11, s1
	s_add_i32 s60, s10, s11
	s_lshl_b64 s[10:11], s[60:61], 12
	s_add_u32 s1, s96, s10
	s_addc_u32 s10, s97, s11
	s_lshl_b32 s11, s29, 1
	s_add_u32 s88, s1, s11
	s_addc_u32 s89, s10, 0
	s_and_b64 s[10:11], s[8:9], exec
	s_cselect_b32 s1, 0x800, 0
	s_lshl_b32 s10, s0, 3
	s_and_b32 s10, s10, 0x1f80
	s_add_i32 s60, s10, 0xfffff100
	s_add_i32 s10, s1, s60
	s_mov_b32 s11, s61
	s_lshl_b64 s[10:11], s[10:11], 13
	s_add_u32 s10, s74, s10
	s_addc_u32 s11, s75, s11
	s_add_u32 s10, s10, s13
	s_addc_u32 s11, s11, 0
	v_writelane_b32 v253, s10, 8
	s_nop 1
	v_writelane_b32 v253, s11, 9
	s_lshl_b32 s10, s1, 2
	s_add_u32 s13, s72, s10
	s_addc_u32 s20, s73, 0
	s_lshl_b64 s[10:11], s[60:61], 2
	s_add_u32 s10, s13, s10
	s_addc_u32 s11, s20, s11
	v_writelane_b32 v253, s10, 10
	s_nop 1
	v_writelane_b32 v253, s11, 11
	s_or_b32 s10, s1, s12
	s_lshl_b32 s10, s10, 12
	s_add_u32 s12, s92, s10
	s_addc_u32 s13, s93, 0
	s_lshl_b64 s[10:11], s[60:61], 1
	s_add_u32 s10, s12, s10
	s_addc_u32 s11, s13, s11
	v_writelane_b32 v253, s10, 12
	s_nop 1
	v_writelane_b32 v253, s11, 13
	s_sext_i32_i16 s10, s0
	s_mulk_i32 s10, 0x8889
	s_lshr_b32 s10, s10, 16
	s_add_i32 s10, s10, s0
	s_sext_i32_i16 s11, s10
	s_ashr_i32 s11, s11, 4
	s_bfe_u32 s10, s10, 0x1000f
	s_add_i32 s10, s11, s10
	s_mul_i32 s11, s10, 30
	s_sext_i32_i16 s10, s10
	s_sub_i32 s0, s0, s11
	s_lshl_b32 s10, s10, 7
	s_sext_i32_i16 s90, s0
	s_add_i32 s0, s1, s10
	s_ashr_i32 s11, s10, 31
	s_mul_hi_i32 s12, s0, 0x3c00
	s_mulk_i32 s0, 0x3c00
	s_add_u32 s0, s52, s0
	s_addc_u32 s28, s53, s12
; __device__ __forceinline__ bool tdecode(const Params& p, int it, TDesc& d) {
;     if (it >= 2 * 6880) return false;
;     const int l = it / 6880; int r = it % 6880;
;     d.ksc = nullptr;
;     if (r < 480) { const int kt = r / 30, nt = r % 30;
;         d.src = p.in[6] + ((size_t)l * 2048 + kt * 128) * DIN + nt * 128; d.lds_ = DIN;
;         d.dst = (nt < 4 ? (bf16_t*)(p.ws + WS_WPQ) + ((size_t)l * 512 + nt * 128) * 2048 : (bf16_t*)(p.ws + WS_WIN) + ((size_t)l * NPROJ + (nt - 4) * 128) * 2048) + kt * 128; d.ldd = 2048; return true; }
; __device__ __forceinline__ void ph_mixers(const Params& p, const int l, LAS unsigned char* lds, const int vbx, const int vG) {
;     ...
;     if (vG == 256) { if (vbx < 128) { ufirst = vbx * 2; ucount = 2; } else { ufirst = 256 + (vbx - 128) * 4; ucount = 4; } ustep = 1; }
;     else { ufirst = vbx; ustep = vG; ucount = (768 - vbx + vG - 1) / vG; }
;     const int nsw = (256 - vbx + vG - 1) / vG;
;     const int ngm = vbx < 128 ? (128 - vbx + vG - 1) / vG : 0;
;     const int nitems = ngm + nsw + ucount;
	s_lshl_b32 s12, s90, 7
	s_ashr_i32 s13, s12, 31
	s_lshl_b64 s[20:21], s[12:13], 2
	s_add_u32 s20, s0, s20
	s_addc_u32 s21, s28, s21
	v_writelane_b32 v253, s20, 14
	s_nop 1
	v_writelane_b32 v253, s21, 15
	s_and_b64 s[20:21], s[8:9], exec
	s_cselect_b32 s0, 0xd00, 0
	s_add_i32 s91, s12, s0
	s_addk_i32 s91, 0xfe00
	s_and_b64 s[8:9], s[8:9], exec
	s_cselect_b32 s8, 0x200000, 0
	v_writelane_b32 v253, s38, 16
	s_add_u32 s8, s38, s8
	v_writelane_b32 v253, s39, 17
	s_addc_u32 s9, s39, 0
	v_sub_co_u32_e64 v1, s[38:39], s18, v1
	s_cmpk_gt_i32 s18, 0x1df
	v_readfirstlane_b32 s20, v1
	s_cselect_b64 s[28:29], -1, 0
	s_lshr_b32 s21, s20, 7
	v_writelane_b32 v253, s28, 18
	s_add_i32 s60, s19, s21
	v_sub_co_u32_e64 v1, s[40:41], s18, v2
	s_lshl_b32 s19, s20, 3
	v_writelane_b32 v253, s29, 19
	s_xor_b64 s[28:29], s[40:41], -1
	s_and_b32 s19, s19, 0x380
	s_lshl_b64 s[20:21], s[60:61], 23
	v_writelane_b32 v253, s28, 20
	s_add_u32 s20, s84, s20
	s_addc_u32 s21, s85, s21
	v_writelane_b32 v253, s29, 21
	s_lshl_b32 s28, s19, 13
	s_add_u32 s20, s20, s28
	s_addc_u32 s21, s21, 0
	s_lshl_b32 s28, s18, 7
	s_and_b32 s28, s28, 0x780
	s_lshl_b32 s29, s28, 2
	s_add_u32 s40, s20, s29
	s_addc_u32 s41, s21, 0
	s_lshl_b64 s[20:21], s[60:61], 22
	s_add_u32 s20, s2, s20
	s_addc_u32 s21, s44, s21
	s_lshl_b32 s31, s28, 11
	s_add_u32 s20, s20, s31
	s_addc_u32 s21, s21, 0
	s_lshl_b32 s19, s19, 1
	s_add_u32 s48, s20, s19
	s_addc_u32 s49, s21, 0
	s_and_b32 s19, s18, 7
	v_readfirstlane_b32 s20, v1
	s_cmpk_lt_u32 s20, 0x800
	s_cselect_b32 s21, s81, s83
	s_cselect_b32 s31, s80, s82
	s_lshl_b32 s47, s20, 4
	s_and_b32 s56, s47, 0x7800
	s_or_b32 s46, s33, s56
	s_and_b32 s47, s47, 0x780
	s_or_b32 s56, s46, s47
	s_lshl_b32 s56, s56, 12
	s_add_u32 s31, s31, s56
	s_addc_u32 s21, s21, 0
	s_lshl_b32 s56, s19, 9
	s_add_u32 s94, s31, s56
	s_addc_u32 s95, s21, 0
	s_lshr_b32 s20, s20, 4
	s_lshl_b32 s19, s19, 8
	s_and_b32 s20, s20, 0xfffff80
	s_add_i32 s20, s20, s19
	s_add_i32 s60, s46, s20
	s_lshl_b64 s[20:21], s[60:61], 12
	v_writelane_b32 v253, s2, 22
	s_add_u32 s19, s96, s20
	v_writelane_b32 v253, s44, 23
	s_addc_u32 s20, s97, s21
	s_lshl_b32 s21, s47, 1
	v_writelane_b32 v253, s96, 24
	s_add_u32 s96, s19, s21
	v_writelane_b32 v253, s97, 25
	s_addc_u32 s97, s20, 0
	s_lshl_b32 s19, s18, 3
	s_and_b32 s19, s19, 0x1f80
	s_add_i32 s60, s19, 0xfffff100
	s_add_i32 s20, s1, s60
	s_mov_b32 s21, s61
	s_lshl_b64 s[20:21], s[20:21], 13
	s_add_u32 s19, s74, s20
	s_addc_u32 s20, s75, s21
	s_add_u32 s44, s19, s29
	s_addc_u32 s45, s20, 0
	s_or_b32 s19, s1, s28
	s_lshl_b32 s19, s19, 12
	s_add_u32 s19, s92, s19
	v_writelane_b32 v253, s44, 26
	s_addc_u32 s28, s93, 0
	s_lshl_b64 s[20:21], s[60:61], 1
	v_writelane_b32 v253, s45, 27
	s_add_u32 s20, s19, s20
	s_sext_i32_i16 s19, s18
	v_writelane_b32 v253, s92, 28
	s_mulk_i32 s19, 0x8889
	v_writelane_b32 v253, s93, 29
	s_addc_u32 s21, s28, s21
	s_lshr_b32 s19, s19, 16
	v_writelane_b32 v253, s20, 30
	s_add_i32 s19, s19, s18
	v_readlane_b32 s33, v250, 51
	v_writelane_b32 v253, s21, 31
	s_sext_i32_i16 s20, s19
	s_ashr_i32 s20, s20, 4
	s_bfe_u32 s19, s19, 0x1000f
	s_add_i32 s19, s20, s19
	s_mul_i32 s20, s19, 30
	s_sub_i32 s18, s18, s20
	s_sext_i32_i16 s19, s19
	s_sext_i32_i16 s56, s18
	s_lshl_b32 s18, s19, 7
	s_add_i32 s1, s1, s18
	s_ashr_i32 s19, s18, 31
	s_mul_hi_i32 s20, s1, 0x3c00
	s_mulk_i32 s1, 0x3c00
	s_add_u32 s1, s52, s1
	s_addc_u32 s28, s53, s20
	s_lshl_b32 s20, s56, 7
	s_ashr_i32 s21, s20, 31
	s_lshl_b64 s[46:47], s[20:21], 2
	s_add_u32 s44, s1, s46
	s_addc_u32 s45, s28, s47
	v_writelane_b32 v253, s44, 32
	s_add_i32 s60, s20, s0
	s_addk_i32 s60, 0xfe00
	v_writelane_b32 v253, s45, 33
	s_lshl_b32 s0, s30, 1
	v_writelane_b32 v253, s0, 34
	s_add_u32 s0, s26, 0x200000
	s_addc_u32 s1, s27, 0
	v_writelane_b32 v253, s0, 35
	v_readlane_b32 s2, v249, 28
	s_mov_b64 s[46:47], s[62:63]
	v_writelane_b32 v253, s1, 36
	s_add_u32 s0, s26, 0x204000
	s_addc_u32 s1, s27, 0
	v_writelane_b32 v253, s0, 37
	v_mbcnt_lo_u32_b32 v1, -1, 0
	v_mbcnt_hi_u32_b32 v212, -1, v1
	v_writelane_b32 v253, s1, 38
	s_add_u32 s0, s26, 0x208000
	s_addc_u32 s1, s27, 0
	v_writelane_b32 v253, s0, 39
	v_and_b32_e32 v226, 64, v212
	v_add_u32_e32 v213, 64, v226
	v_writelane_b32 v253, s1, 40
	s_add_u32 s0, s26, 0x2a800000
	s_addc_u32 s1, s27, 0
	v_writelane_b32 v253, s0, 41
	v_xor_b32_e32 v220, 1, v212
	v_xor_b32_e32 v216, 16, v212
	v_writelane_b32 v253, s1, 42
	s_add_u32 s0, s26, 0x20a000
	s_addc_u32 s1, s27, 0
	v_writelane_b32 v253, s0, 43
	s_nop 1
	v_writelane_b32 v253, s1, 44
	v_readlane_b32 s0, v249, 28
	s_cmpk_lt_i32 s0, 0x100
	s_cselect_b64 s[0:1], -1, 0
	v_writelane_b32 v253, s0, 45
	s_nop 1
	v_writelane_b32 v253, s1, 46
	v_readlane_b32 s0, v249, 28
	s_ashr_i32 s30, s0, 6
	s_ashr_i32 s31, s30, 31
	s_lshl_b64 s[30:31], s[30:31], 21
	s_add_u32 s0, s33, s30
	s_addc_u32 s1, s3, s31
	s_lshl_b32 s28, s2, 15
	s_and_b32 s28, s28, 0x1f8000
	s_add_u32 s0, s0, s28
	v_writelane_b32 v253, s3, 47
	s_addc_u32 s1, s1, 0
	v_writelane_b32 v253, s0, 48
	s_nop 1
	v_writelane_b32 v253, s1, 49
	v_readlane_b32 s0, v249, 28
	s_lshl_b32 s0, s0, 2
	v_readlane_b32 s1, v249, 28
	s_addk_i32 s0, 0xff00
	s_lshl_b32 s44, s1, 1
	s_and_b64 s[30:31], vcc, exec
	s_cmpk_lt_u32 s1, 0x80
	s_cselect_b32 s0, s44, s0
	v_writelane_b32 v253, s0, 50
	s_cselect_b32 s0, 2, 4
	v_writelane_b32 v253, s0, 51
	v_readlane_b32 s0, v249, 28
	s_sub_i32 s0, 0x100, s0
	s_nop 0
	v_writelane_b32 v253, s0, 52
	s_add_u32 s0, s26, 0x3b300000
	v_writelane_b32 v253, s0, 53
	s_addc_u32 s0, s27, 0
	v_writelane_b32 v253, s0, 54
	s_add_u32 s0, s26, 0x2d800000
	s_addc_u32 s1, s27, 0
	v_writelane_b32 v253, s0, 55
	s_nop 1
	v_writelane_b32 v253, s1, 56
	s_add_u32 s0, s26, 0x2f000000
;     __device__ __forceinline__ bool next(int i, GUnit& u) const {
;         const int L = i * G + c; if (L >= 512) return false;
;         const int Lp = (L & 7) * 64 + (L >> 3);
;         const int e = Lp >> 5, r = Lp & 31, pm = r & 3, pn = r >> 2;
;         u.pm = e * 4 + pm; u.pn = pn; u.z = e;
;         u.a = A; u.b = B + ((size_t)e * 2048 + pn * 256) * K * 2; return true;
; __global__ void __launch_bounds__(512, 2) mk_fwd(Params p) {
;     ...
;         } else if (EN(12) && IN(pb + 6)) {
;             __syncthreads();
;             ph_topk(p, lds, (const unsigned*)(p.ws + WS_CTL) + CTL_PANEL + 4096 + 1024 + (size_t)l * 1024);
;             if (split_ok && l == 0 && bx >= 64 && bx < 68) ph_rbias(p, 1, bx - 64);
	s_addc_u32 s1, s27, 0
	v_writelane_b32 v253, s0, 57
	s_nop 1
	v_writelane_b32 v253, s1, 58
	s_add_u32 s0, s26, 0x2d000000
	s_addc_u32 s1, s27, 0
	v_writelane_b32 v253, s0, 59
	s_nop 1
	v_writelane_b32 v253, s1, 60
	s_add_u32 s0, s26, 0x2c800000
	s_addc_u32 s1, s27, 0
	v_writelane_b32 v253, s0, 61
	s_nop 1
	v_writelane_b32 v253, s1, 62
	s_add_u32 s0, s26, 0x3b3e0000
	s_addc_u32 s1, s27, 0
	v_writelane_b32 v253, s0, 63
	s_nop 1
	v_writelane_b32 v254, s1, 0
	s_add_u32 s0, s26, 0x3b3a0000
	s_addc_u32 s1, s27, 0
	s_add_u32 s72, s26, 0x2f100000
	v_writelane_b32 v254, s0, 1
	s_addc_u32 s73, s27, 0
	s_nop 0
	v_writelane_b32 v254, s1, 2
	s_add_u32 s0, s26, 0x31300000
	v_writelane_b32 v254, s0, 3
	s_addc_u32 s0, s27, 0
	v_writelane_b32 v254, s0, 4
	s_add_u32 s0, s26, 0x31100000
	s_addc_u32 s1, s27, 0
	v_writelane_b32 v254, s0, 5
	s_nop 1
	v_writelane_b32 v254, s1, 6
	s_add_u32 s0, s26, 0x8000
	v_writelane_b32 v254, s0, 7
	s_addc_u32 s0, s27, 0
	v_writelane_b32 v254, s0, 8
	s_add_u32 s0, s26, 0xd000
	v_writelane_b32 v254, s0, 9
	s_addc_u32 s0, s27, 0
	s_add_u32 s2, s26, 0x31200000
	s_addc_u32 s3, s27, 0
	s_add_u32 s62, s26, 0x31210000
	v_writelane_b32 v254, s0, 10
	s_addc_u32 s63, s27, 0
	v_readlane_b32 s0, v249, 28
	s_cmp_lt_i32 s0, 64
	s_cselect_b64 s[0:1], -1, 0
	v_writelane_b32 v254, s0, 11
	s_nop 1
	v_writelane_b32 v254, s1, 12
	v_readlane_b32 s0, v249, 28
	s_and_b32 s0, s0, -4
	s_cmp_eq_u32 s0, 64
	s_cselect_b64 s[0:1], -1, 0
	v_writelane_b32 v254, s0, 13
	s_nop 1
	v_writelane_b32 v254, s1, 14
	v_readlane_b32 s0, v249, 28
	s_add_u32 s30, s0, 0xffffffc4
	s_addc_u32 s31, 0, -1
	s_mul_hi_u32 s0, s30, 0xc000
	s_mul_i32 s1, s31, 0xc000
	s_add_i32 s0, s0, s1
	s_mul_i32 s1, s30, 0xc000
	s_add_u32 s1, s26, s1
	s_addc_u32 s0, s27, s0
	s_add_u32 s28, s1, 0x106000
	s_addc_u32 s29, s0, 0
	v_writelane_b32 v254, s28, 15
	s_add_u32 s0, s26, 0x3b390000
	s_addc_u32 s1, s27, 0
	v_writelane_b32 v254, s29, 16
	v_writelane_b32 v254, s0, 17
	s_lshl_b64 s[30:31], s[30:31], 6
	s_nop 0
	v_writelane_b32 v254, s1, 18
	v_writelane_b32 v254, s7, 19
	s_add_u32 s0, s7, s30
	v_writelane_b32 v254, s43, 20
	s_addc_u32 s1, s43, s31
	v_writelane_b32 v254, s0, 21
	s_add_u32 s52, s26, 0x35300000
	s_addc_u32 s53, s27, 0
	v_writelane_b32 v254, s1, 22
	v_readlane_b32 s0, v249, 28
	s_cmpk_lt_i32 s0, 0x200
	s_cselect_b64 s[0:1], -1, 0
	v_writelane_b32 v254, s0, 23
	s_mov_b32 s31, s33
	s_mul_i32 s43, s58, 6
	v_writelane_b32 v254, s1, 24
	v_readlane_b32 s0, v249, 28
	s_lshl_b32 s0, s0, 6
	v_readlane_b32 s1, v249, 28
	s_and_b32 s0, s0, 0x1c0
	s_ashr_i32 s1, s1, 3
	s_add_i32 s0, s0, s1
	s_bfe_u32 s30, s1, 0x30002
	s_ashr_i32 s0, s0, 5
	s_and_b32 s28, s1, 3
	s_lshl_b32 s1, s0, 2
	s_lshl_b32 s33, s30, 20
	s_or_b32 s29, s1, s28
	v_writelane_b32 v254, s33, 25
	v_writelane_b32 v254, s29, 26
	s_lshl_b32 s29, s29, 8
	s_ashr_i32 s1, s0, 31
	v_writelane_b32 v254, s29, 27
	s_bitset1_b32 s29, 7
	v_writelane_b32 v254, s29, 28
	s_lshl_b64 s[74:75], s[0:1], 23
	v_writelane_b32 v254, s74, 29
	s_mov_b32 s7, 0x42b17218
	s_nop 0
	v_writelane_b32 v254, s75, 30
	s_add_u32 s74, s26, 0x24400080
	s_addc_u32 s75, s27, 0
	v_writelane_b32 v254, s74, 31
	s_lshl_b32 s33, s28, 19
	s_lshl_b64 s[28:29], s[0:1], 21
	v_writelane_b32 v254, s75, 32
	s_add_u32 s28, s52, s28
	v_writelane_b32 v254, s52, 33
	s_addc_u32 s29, s53, s29
	s_add_u32 s28, s28, s33
	v_writelane_b32 v254, s53, 34
	s_addc_u32 s29, s29, 0
	v_writelane_b32 v254, s28, 35
	s_lshl_b64 s[0:1], s[0:1], 22
	v_readlane_b32 s52, v249, 57
	v_writelane_b32 v254, s29, 36
	v_writelane_b32 v254, s0, 37
	v_readlane_b32 s53, v249, 58
	s_nop 0
	v_writelane_b32 v254, s1, 38
	v_writelane_b32 v254, s30, 39
	s_lshl_b32 s0, s30, 19
	v_writelane_b32 v254, s0, 40
	v_readlane_b32 s0, v249, 28
	s_cmpk_lt_i32 s0, 0x1a0
	s_cselect_b64 s[0:1], -1, 0
	v_writelane_b32 v254, s0, 41
	v_readlane_b32 s30, v249, 28
	s_nop 0
	v_writelane_b32 v254, s1, 42
	s_and_b64 s[0:1], s[0:1], exec
	v_readlane_b32 s0, v250, 58
	s_cselect_b32 s0, s4, s0
	v_readlane_b32 s1, v251, 0
	v_writelane_b32 v254, s0, 43
	v_readlane_b32 s0, v250, 59
	s_cselect_b32 s0, s1, s0
	v_readlane_b32 s4, v252, 37
	v_writelane_b32 v254, s0, 44
	v_readlane_b32 s0, v252, 24
	v_readlane_b32 s1, v252, 25
	s_and_b64 s[0:1], s[0:1], exec
	v_readlane_b32 s0, v252, 31
	v_readlane_b32 s1, v252, 38
	s_cselect_b32 s1, s1, s0
	v_readlane_b32 s0, v252, 30
	s_cselect_b32 s0, s4, s0
	v_readlane_b32 s4, v252, 39
	v_writelane_b32 v254, s0, 45
	v_writelane_b32 v251, s54, 0
	s_nop 0
	v_writelane_b32 v254, s1, 46
	v_readlane_b32 s0, v252, 35
	v_readlane_b32 s1, v252, 40
	s_cselect_b32 s1, s1, s0
	v_readlane_b32 s0, v252, 33
	s_cselect_b32 s0, s4, s0
	s_movk_i32 s4, 0x400
	v_writelane_b32 v254, s0, 47
	v_writelane_b32 v251, s55, 1
	s_nop 0
	v_writelane_b32 v254, s1, 48
	s_cselect_b32 s0, 0x800, s4
	v_writelane_b32 v254, s0, 49
	s_cselect_b32 s0, s4, 0x800
	v_writelane_b32 v254, s0, 50
	s_nop 1
	v_writelane_b32 v254, s1, 51
	v_readlane_b32 s0, v252, 49
	s_cmp_lt_u32 s0, 4
	s_cselect_b32 s0, s64, s5
	s_cselect_b32 s1, 0, s22
	s_cselect_b32 s5, s59, s15
	s_cselect_b32 s22, s23, s14
	s_lshl_b64 s[0:1], s[0:1], 12
	s_add_u32 s0, s22, s0
	s_addc_u32 s1, s5, s1
	s_lshl_b32 s5, s34, 1
	s_add_u32 s0, s0, s5
	s_addc_u32 s1, s1, 0
	v_writelane_b32 v254, s0, 52
	s_nop 1
	v_writelane_b32 v254, s1, 53
	v_readlane_b32 s0, v252, 50
	v_readlane_b32 s1, v252, 51
	s_and_b64 s[0:1], s[0:1], exec
	v_readlane_b32 s0, v252, 58
	s_cselect_b32 s1, s70, s35
	s_cselect_b32 s0, s0, s79
	v_writelane_b32 v254, s0, 54
	s_nop 1
	v_writelane_b32 v254, s1, 55
	v_readlane_b32 s0, v252, 57
	s_cselect_b32 s1, s76, s0
	v_readlane_b32 s0, v252, 56
	s_cselect_b32 s0, s71, s0
	s_nop 0
; #define LAS __attribute__((address_space(3)))
; __device__ __forceinline__ int opaque_tid() { int t = threadIdx.x; asm volatile("" : "+v"(t)); return t; }
; __device__ __forceinline__ void ph_mixers(const Params& p, const int l, LAS unsigned char* lds, const int vbx, const int vG) {
;     constexpr int VTS = 260, VTSS = 292, KSTR = 72, ARENA = 78848, KOFF = 37376;
;     const int hw = (opaque_tid() >> 8) & 1;
;     const bf16_t* PROJ = (const bf16_t*)(p.ws + WS_PROJ);
;     int ufirst, ucount, ustep;
;     if (vG == 256) { if (vbx < 128) { ufirst = vbx * 2; ucount = 2; } else { ufirst = 256 + (vbx - 128) * 4; ucount = 4; } ustep = 1; }
;     else { ufirst = vbx; ustep = vG; ucount = (768 - vbx + vG - 1) / vG; }
;     const int nsw = (256 - vbx + vG - 1) / vG;
;     const int ngm = vbx < 128 ? (128 - vbx + vG - 1) / vG : 0;
;     const int nitems = ngm + nsw + ucount;
; __global__ void __launch_bounds__(512, 2) mk_fwd(Params p) {
;     ...
;     volatile LAS unsigned* misc = (volatile LAS unsigned*)(lds + MISC_OFF);
;     if (tid < 16) misc[tid] = 0u;
;     __syncthreads();
;     const int lo = p.ph_lo, hi = p.ph_hi;
;     XcdBarrier bar; bar.bar = (unsigned*)(p.ws + WS_CTL); bar.x = 0; bar.st = misc + 8; bar.gsz = (unsigned)G;
;     if (hi - lo > 1) bar = xcd_barrier_post((unsigned*)(p.ws + WS_CTL), misc + 8, (unsigned)G);
;     const bool split_ok = (G == 256) && (hi - lo > 1);
;     XcdBarrier bar2; bar2.bar = (unsigned*)(p.ws + WS_CTL) + 4096; bar2.x = 0; bar2.st = misc + 12; bar2.gsz = (unsigned)MIX_GW;
;     if (split_ok && bx < MIX_GW) bar2 = xcd_barrier_post((unsigned*)(p.ws + WS_CTL) + 4096, misc + 12, (unsigned)MIX_GW);
	v_writelane_b32 v254, s0, 56
	s_nop 1
	v_writelane_b32 v254, s1, 57
	s_cselect_b32 s0, 0x800, s4
	v_writelane_b32 v254, s0, 58
	s_cselect_b32 s0, s4, 0x800
	v_writelane_b32 v254, s0, 59
	s_cmp_lt_u32 s69, 4
	s_cselect_b32 s5, s59, s15
	v_writelane_b32 v254, s1, 60
	s_cselect_b32 s0, s65, s78
	s_cselect_b32 s1, 0, s68
	s_cselect_b32 s22, s23, s14
	s_lshl_b64 s[0:1], s[0:1], 12
	s_add_u32 s0, s22, s0
	s_addc_u32 s1, s5, s1
	s_lshl_b32 s5, s77, 1
	s_add_u32 s0, s0, s5
	s_addc_u32 s1, s1, 0
	v_writelane_b32 v254, s0, 61
	s_mov_b64 s[64:65], 0x80
	s_nop 0
	v_writelane_b32 v254, s1, 62
	s_and_b64 s[0:1], s[66:67], exec
	s_cselect_b32 s1, s57, s87
	s_cselect_b32 s0, s37, s86
	v_writelane_b32 v254, s0, 63
	s_nop 1
	v_writelane_b32 v255, s1, 0
	s_cselect_b32 s1, s89, s36
	s_cselect_b32 s0, s88, s6
	v_writelane_b32 v255, s0, 1
	s_movk_i32 s6, 0x1a00
	s_nop 0
	v_writelane_b32 v255, s1, 2
	s_cselect_b32 s0, 0x800, s4
	v_writelane_b32 v255, s0, 3
	s_cselect_b32 s0, s4, 0x800
	v_writelane_b32 v255, s0, 4
	s_cmp_lt_i32 s90, 4
	s_cselect_b32 s5, s9, s15
	v_writelane_b32 v255, s1, 5
	s_cselect_b32 s0, s12, s91
	s_cselect_b32 s1, s13, 0
	s_cselect_b32 s12, s8, s14
	s_lshl_b64 s[0:1], s[0:1], 12
	s_add_u32 s12, s12, s0
	s_addc_u32 s5, s5, s1
	s_lshl_b64 s[0:1], s[10:11], 1
	s_add_u32 s0, s12, s0
	s_addc_u32 s1, s5, s1
	v_writelane_b32 v255, s0, 6
	s_nop 1
	v_writelane_b32 v255, s1, 7
	s_and_b64 s[0:1], s[38:39], exec
	s_cselect_b32 s1, s95, s41
	s_cselect_b32 s0, s94, s40
	v_writelane_b32 v255, s0, 8
	s_nop 1
	v_writelane_b32 v255, s1, 9
	s_cselect_b32 s1, s97, s49
	s_cselect_b32 s0, s96, s48
	v_writelane_b32 v255, s0, 10
	s_nop 1
	v_writelane_b32 v255, s1, 11
	s_cselect_b32 s0, 0x800, s4
	v_writelane_b32 v255, s0, 12
	s_cselect_b32 s0, s4, 0x800
	v_writelane_b32 v255, s0, 13
	s_cmp_lt_i32 s56, 4
	s_cselect_b32 s4, s9, s15
	v_writelane_b32 v255, s1, 14
	s_cselect_b32 s0, s20, s60
	s_cselect_b32 s1, s21, 0
	v_writelane_b32 v252, s14, 31
	s_cselect_b32 s5, s8, s14
	s_lshl_b64 s[0:1], s[0:1], 12
	s_add_u32 s5, s5, s0
	s_addc_u32 s4, s4, s1
	s_lshl_b64 s[0:1], s[18:19], 1
	s_add_u32 s0, s5, s0
	s_addc_u32 s1, s4, s1
	v_writelane_b32 v255, s0, 15
	v_writelane_b32 v252, s15, 32
	v_readlane_b32 s20, v250, 4
	v_writelane_b32 v255, s1, 16
	v_readlane_b32 s0, v249, 52
	s_add_i32 s0, s0, s42
	s_ashr_i32 s1, s0, 31
	s_lshr_b32 s1, s1, 26
	s_add_i32 s1, s0, s1
	s_and_b32 s4, s1, 0xffc0
	s_sub_i32 s0, s0, s4
	s_bfe_i32 s4, s0, 0x80000
	s_bfe_u32 s4, s4, 0x3000c
	s_add_i32 s4, s0, s4
	s_and_b32 s5, s4, 0xf8
	s_sub_i32 s0, s0, s5
	s_ashr_i32 s1, s1, 6
	s_bfe_i32 s4, s4, 0x80000
	s_lshl_b32 s1, s1, 3
	s_sext_i32_i16 s4, s4
	s_sext_i32_i8 s0, s0
	s_add_i32 s8, s1, s0
	s_ashr_i32 s0, s4, 3
	v_writelane_b32 v255, s0, 17
	s_lshr_b32 s0, s4, 3
	s_mov_b32 s4, s8
	s_ashr_i32 s9, s8, 31
	v_writelane_b32 v255, s4, 18
	s_mul_i32 s42, s58, 3
	v_readlane_b32 s14, v250, 49
	v_writelane_b32 v255, s5, 19
	s_lshl_b64 s[4:5], s[8:9], 20
	s_add_u32 s4, s72, s4
	v_writelane_b32 v255, s72, 20
	s_addc_u32 s5, s73, s5
	s_bfe_i64 s[0:1], s[0:1], 0x100000
	v_writelane_b32 v255, s73, 21
	v_writelane_b32 v255, s4, 22
	s_lshl_b64 s[0:1], s[0:1], 20
	v_readlane_b32 s18, v249, 60
	v_writelane_b32 v255, s5, 23
	v_writelane_b32 v255, s0, 24
	s_add_i32 s4, s43, 0xfffffde1
	v_readlane_b32 s21, v249, 59
	v_writelane_b32 v255, s1, 25
	s_add_i32 s0, s30, s42
	s_lshl_b32 s0, s0, 1
	s_addk_i32 s0, 0xfde0
	v_writelane_b32 v255, s0, 26
	s_mul_i32 s0, s58, 0x300
	s_add_i32 s1, s0, 0xfffef000
	v_writelane_b32 v255, s1, 27
	s_add_i32 s0, s0, 0xfffef080
	v_writelane_b32 v255, s0, 28
	s_add_i32 s0, s43, 0xffffeb00
	v_writelane_b32 v255, s0, 29
	s_add_i32 s0, s43, 0xfffffb00
	v_writelane_b32 v255, s0, 30
	s_add_i32 s0, s43, 0xfffffde0
	v_writelane_b32 v255, s0, 31
	s_add_i32 s0, s43, 0xffffeb01
	v_writelane_b32 v255, s0, 32
	s_add_i32 s0, s43, 0xfffffb01
	v_writelane_b32 v255, s0, 33
	s_mul_i32 s0, s58, 0x60
	s_add_i32 s1, s0, 0xffffb000
	v_writelane_b32 v255, s1, 34
	s_addk_i32 s0, 0xb010
	v_writelane_b32 v255, s0, 35
	s_mul_i32 s0, s58, 48
	s_add_i32 s1, s0, 0xffff5800
	v_writelane_b32 v255, s1, 36
	s_add_i32 s1, s0, 0xffffef00
	v_writelane_b32 v255, s1, 37
	s_add_i32 s1, s0, 0xffff5808
	v_writelane_b32 v255, s1, 38
	s_addk_i32 s0, 0xef08
	v_writelane_b32 v255, s0, 39
	s_add_i32 s0, s42, 0xfffffef0
	v_writelane_b32 v252, s0, 37
	s_lshl_b32 s0, s58, 1
	s_add_i32 s1, s30, s0
	s_lshl_b32 s1, s1, 1
	s_addk_i32 s1, 0xfee0
	v_writelane_b32 v255, s1, 40
	s_lshl_b32 s1, s58, 9
	s_add_i32 s5, s1, 0xffff0000
	v_writelane_b32 v252, s5, 38
	s_add_i32 s5, s1, 0xffff7000
	v_writelane_b32 v255, s5, 41
	s_add_i32 s1, s1, 0xffff7080
	v_writelane_b32 v255, s1, 42
	s_lshl_b32 s1, s58, 2
	s_add_i32 s5, s1, 0xfffffe00
	v_writelane_b32 v252, s5, 39
	s_add_i32 s5, s1, 0xffffec00
	v_writelane_b32 v255, s5, 43
	s_add_i32 s5, s1, 0xfffffc00
	v_writelane_b32 v255, s5, 44
	s_add_i32 s5, s1, 0xfffffee0
	s_add_i32 s8, s1, 0xffffec01
	v_writelane_b32 v252, s5, 50
	s_add_i32 s5, s1, 0xfffffee1
	v_writelane_b32 v255, s8, 45
	s_addk_i32 s1, 0xfc01
	v_writelane_b32 v255, s1, 46
	s_lshl_b32 s1, s58, 6
	s_add_i32 s8, s1, 0xffffe000
	v_writelane_b32 v252, s8, 40
	s_add_i32 s8, s1, 0xffffc000
	v_writelane_b32 v255, s8, 47
	s_addk_i32 s1, 0xc010
	s_addk_i32 s0, 0xff70
	v_writelane_b32 v255, s1, 48
	v_writelane_b32 v252, s0, 30
	s_lshl_b32 s0, s30, 4
	v_writelane_b32 v255, s0, 49
	s_add_i32 s0, s20, 0xfffff000
	v_writelane_b32 v252, s0, 49
	s_lshl_b32 s0, s30, 8
	v_writelane_b32 v255, s0, 50
	v_writelane_b32 v255, s4, 51
	s_add_i32 s0, s4, s44
	v_writelane_b32 v255, s0, 52
	s_add_i32 s0, s20, 0xffff6000
	v_writelane_b32 v255, s0, 53
	s_add_i32 s0, s20, 0xfffff700
	v_writelane_b32 v255, s0, 54
	s_add_i32 s0, s20, 0xffff6008
	v_writelane_b32 v255, s0, 55
	v_writelane_b32 v255, s44, 56
	s_add_i32 s0, s5, s44
	v_writelane_b32 v255, s0, 57
	s_add_i32 s0, s20, 0xfffff708
	v_writelane_b32 v255, s0, 58
	s_add_i32 s0, 0, 0x27f20
	v_writelane_b32 v252, s0, 56
	s_add_i32 s0, 0, 0x27f24
	v_writelane_b32 v252, s0, 57
	v_cmp_eq_u32_e64 s[8:9], 0, v0
	s_add_i32 s0, 0, 0x27f30
	v_writelane_b32 v255, s0, 59
	v_writelane_b32 v252, s8, 33
	s_add_i32 s0, 0, 0x27f34
	v_readlane_b32 s15, v250, 50
	v_writelane_b32 v252, s9, 34
	v_writelane_b32 v252, s46, 24
	v_readlane_b32 s19, v249, 61
	v_writelane_b32 v250, s5, 58
	s_mov_b32 s5, 0xf800000
	s_movk_i32 s43, 0x4000
	v_writelane_b32 v255, s0, 60
	s_mov_b32 s1, 0x5040100
	s_mov_b32 s0, s61
	v_writelane_b32 v252, s47, 25
	s_branch .LBB0_333

; __device__ __forceinline__ float bflo(unsigned u) { return __uint_as_float(u << 16); }
; __device__ __forceinline__ float bfhi(unsigned u) { return __uint_as_float(u & 0xffff0000u); }
; __device__ __forceinline__ int opaque_tid() { int t = threadIdx.x; asm volatile("" : "+v"(t)); return t; }
; __device__ __forceinline__ void ph_rbias(const Params& p, const int l, const int b) {
;     const int tid = opaque_tid(), e = tid >> 5, part = tid & 31;
;     const float* sh = (const float*)(p.ws + WS_MOD) + ((size_t)l * 4 + b) * 12288 + 3 * 2048 + part * 64;
;     const bf16_t* w = (const bf16_t*)(p.ws + WS_WRT) + ((size_t)l * 16 + e) * 2048 + part * 64;
;     float s = 0.f;
; #pragma unroll
;     for (int i = 0; i < 8; ++i) {
;         const u32x4 wv = *(const u32x4*)(w + 8 * i); const f32x4 s0 = *(const f32x4*)(sh + 8 * i), s1 = *(const f32x4*)(sh + 8 * i + 4);
;         s += (s0[0] * bflo(wv.x) + s0[1] * bfhi(wv.x)) + (s0[2] * bflo(wv.y) + s0[3] * bfhi(wv.y)) + (s1[0] * bflo(wv.z) + s1[1] * bfhi(wv.z)) + (s1[2] * bflo(wv.w) + s1[3] * bfhi(wv.w));
;     }
; #pragma unroll
;     for (int o = 1; o < 32; o <<= 1) s += __shfl_xor(s, o);
;     if (part == 0) ((float*)(p.ws + WS_XE + 16 * MiB))[((size_t)l * 4 + b) * 16 + e] = s;
.Lcv_rb775:
	v_readlane_b32 s8, v252, 16
	v_readlane_b32 s9, v252, 17
	s_andn2_b64 vcc, exec, s[8:9]
	s_cbranch_vccnz .LBB0_779
	v_mov_b32_e32 v1, v0
	v_readlane_b32 s8, v249, 55
	s_waitcnt vmcnt(0)
	v_ashrrev_i32_e32 v26, 5, v1
	s_waitcnt lgkmcnt(0)
	v_ashrrev_i32_e32 v27, 31, v26
	v_and_b32_e32 v1, 31, v1
	v_lshlrev_b64 v[2:3], 12, v[26:27]
	v_readlane_b32 s9, v249, 56
	v_lshlrev_b32_e32 v194, 7, v1
	v_lshlrev_b32_e32 v22, 8, v1
	v_lshl_add_u64 v[2:3], s[8:9], 0, v[2:3]
	v_lshl_add_u64 v[10:11], v[2:3], 0, v[194:195]
	v_readlane_b32 s8, v252, 18
	global_load_dwordx4 v[2:5], v[10:11], off offset:48
	global_load_dwordx4 v[6:9], v[10:11], off offset:32
	global_load_dwordx4 v[12:15], v[10:11], off offset:16
	global_load_dwordx4 v[16:19], v[10:11], off
	v_readlane_b32 s9, v252, 19
	s_nop 4
	global_load_dwordx4 v[28:31], v22, s[8:9] offset:48
	global_load_dwordx4 v[32:35], v22, s[8:9] offset:32
	global_load_dwordx4 v[36:39], v22, s[8:9] offset:16
	global_load_dwordx4 v[40:43], v22, s[8:9]
	v_cmp_lt_i32_e32 vcc, v220, v213
	s_waitcnt vmcnt(6)
	v_lshlrev_b32_e32 v21, 16, v6
	v_and_b32_e32 v6, 0xffff0000, v6
	s_waitcnt vmcnt(4)
	v_lshlrev_b32_e32 v20, 16, v16
	v_and_b32_e32 v16, 0xffff0000, v16
	s_waitcnt vmcnt(0)
	v_mul_f32_e32 v16, v41, v16
	v_fmac_f32_e32 v16, v40, v20
	v_lshlrev_b32_e32 v20, 16, v17
	v_and_b32_e32 v17, 0xffff0000, v17
	v_mul_f32_e32 v17, v43, v17
	v_fmac_f32_e32 v17, v42, v20
	v_add_f32_e32 v16, v16, v17
	v_lshlrev_b32_e32 v17, 16, v18
	v_and_b32_e32 v18, 0xffff0000, v18
	v_mul_f32_e32 v18, v37, v18
	v_fmac_f32_e32 v18, v36, v17
	v_add_f32_e32 v16, v18, v16
	v_and_b32_e32 v18, 0xffff0000, v19
	v_lshlrev_b32_e32 v17, 16, v19
	v_mul_f32_e32 v18, v39, v18
	v_fmac_f32_e32 v18, v38, v17
	v_lshlrev_b32_e32 v17, 16, v12
	v_and_b32_e32 v12, 0xffff0000, v12
	v_mul_f32_e32 v12, v33, v12
	v_fmac_f32_e32 v12, v32, v17
	v_lshlrev_b32_e32 v17, 16, v13
	v_and_b32_e32 v13, 0xffff0000, v13
	v_mul_f32_e32 v13, v35, v13
	v_fmac_f32_e32 v13, v34, v17
	v_add_f32_e32 v12, v12, v13
	v_lshlrev_b32_e32 v13, 16, v14
	v_and_b32_e32 v14, 0xffff0000, v14
	v_mul_f32_e32 v14, v29, v14
	v_fmac_f32_e32 v14, v28, v13
	v_add_f32_e32 v12, v14, v12
	v_and_b32_e32 v14, 0xffff0000, v15
	v_lshlrev_b32_e32 v13, 16, v15
	v_mul_f32_e32 v14, v31, v14
	v_add_f32_e32 v16, v18, v16
	v_fmac_f32_e32 v14, v30, v13
	v_add_f32_e32 v16, 0, v16
	v_add_f32_e32 v12, v14, v12
	v_add_f32_e32 v20, v16, v12
	global_load_dwordx4 v[12:15], v22, s[8:9] offset:112
	global_load_dwordx4 v[16:19], v22, s[8:9] offset:96
	global_load_dwordx4 v[28:31], v22, s[8:9] offset:80
	global_load_dwordx4 v[32:35], v22, s[8:9] offset:64
	s_waitcnt vmcnt(0)
	v_mul_f32_e32 v6, v33, v6
	v_fmac_f32_e32 v6, v32, v21
	v_lshlrev_b32_e32 v21, 16, v7
	v_and_b32_e32 v7, 0xffff0000, v7
	v_mul_f32_e32 v7, v35, v7
	v_fmac_f32_e32 v7, v34, v21
	v_add_f32_e32 v6, v6, v7
	v_lshlrev_b32_e32 v7, 16, v8
	v_and_b32_e32 v8, 0xffff0000, v8
	v_mul_f32_e32 v8, v29, v8
	v_fmac_f32_e32 v8, v28, v7
	v_add_f32_e32 v6, v8, v6
	v_and_b32_e32 v8, 0xffff0000, v9
	v_lshlrev_b32_e32 v7, 16, v9
	v_mul_f32_e32 v8, v31, v8
	v_fmac_f32_e32 v8, v30, v7
	v_lshlrev_b32_e32 v7, 16, v2
	v_and_b32_e32 v2, 0xffff0000, v2
	v_mul_f32_e32 v2, v17, v2
	v_fmac_f32_e32 v2, v16, v7
	v_lshlrev_b32_e32 v7, 16, v3
	v_and_b32_e32 v3, 0xffff0000, v3
	v_mul_f32_e32 v3, v19, v3
	v_fmac_f32_e32 v3, v18, v7
	v_add_f32_e32 v2, v2, v3
	v_lshlrev_b32_e32 v3, 16, v4
	v_and_b32_e32 v4, 0xffff0000, v4
	v_mul_f32_e32 v4, v13, v4
	v_fmac_f32_e32 v4, v12, v3
	v_add_f32_e32 v2, v4, v2
	v_and_b32_e32 v4, 0xffff0000, v5
	v_lshlrev_b32_e32 v3, 16, v5
	v_mul_f32_e32 v4, v15, v4
	v_add_f32_e32 v6, v8, v6
	v_fmac_f32_e32 v4, v14, v3
	v_add_f32_e32 v6, v20, v6
	v_add_f32_e32 v2, v4, v2
	v_add_f32_e32 v20, v6, v2
	global_load_dwordx4 v[2:5], v[10:11], off offset:112
	global_load_dwordx4 v[6:9], v[10:11], off offset:96
	global_load_dwordx4 v[12:15], v[10:11], off offset:80
	global_load_dwordx4 v[16:19], v[10:11], off offset:64
	global_load_dwordx4 v[28:31], v22, s[8:9] offset:176
	global_load_dwordx4 v[32:35], v22, s[8:9] offset:160
	global_load_dwordx4 v[36:39], v22, s[8:9] offset:144
	global_load_dwordx4 v[40:43], v22, s[8:9] offset:128
	s_waitcnt vmcnt(4)
; __device__ __forceinline__ float bflo(unsigned u) { return __uint_as_float(u << 16); }
; __device__ __forceinline__ float bfhi(unsigned u) { return __uint_as_float(u & 0xffff0000u); }
; __device__ __forceinline__ void ph_rbias(const Params& p, const int l, const int b) {
;     ...
;     for (int i = 0; i < 8; ++i) {
;         const u32x4 wv = *(const u32x4*)(w + 8 * i); const f32x4 s0 = *(const f32x4*)(sh + 8 * i), s1 = *(const f32x4*)(sh + 8 * i + 4);
;         s += (s0[0] * bflo(wv.x) + s0[1] * bfhi(wv.x)) + (s0[2] * bflo(wv.y) + s0[3] * bfhi(wv.y)) + (s1[0] * bflo(wv.z) + s1[1] * bfhi(wv.z)) + (s1[2] * bflo(wv.w) + s1[3] * bfhi(wv.w));
;     }
; #pragma unroll
;     for (int o = 1; o < 32; o <<= 1) s += __shfl_xor(s, o);
;     if (part == 0) ((float*)(p.ws + WS_XE + 16 * MiB))[((size_t)l * 4 + b) * 16 + e] = s;
	v_and_b32_e32 v11, 0xffff0000, v16
	v_lshlrev_b32_e32 v10, 16, v16
	v_and_b32_e32 v16, 0xffff0000, v17
	s_waitcnt vmcnt(0)
	v_mul_f32_e32 v11, v41, v11
	v_fmac_f32_e32 v11, v40, v10
	v_lshlrev_b32_e32 v10, 16, v17
	v_mul_f32_e32 v16, v43, v16
	v_fmac_f32_e32 v16, v42, v10
	v_add_f32_e32 v10, v11, v16
	v_and_b32_e32 v16, 0xffff0000, v18
	v_lshlrev_b32_e32 v11, 16, v18
	v_mul_f32_e32 v16, v37, v16
	v_fmac_f32_e32 v16, v36, v11
	v_add_f32_e32 v10, v16, v10
	v_and_b32_e32 v16, 0xffff0000, v19
	v_lshlrev_b32_e32 v11, 16, v19
	v_mul_f32_e32 v16, v39, v16
	v_fmac_f32_e32 v16, v38, v11
	v_lshlrev_b32_e32 v11, 16, v12
	v_and_b32_e32 v12, 0xffff0000, v12
	v_mul_f32_e32 v12, v33, v12
	v_fmac_f32_e32 v12, v32, v11
	v_lshlrev_b32_e32 v11, 16, v13
	v_and_b32_e32 v13, 0xffff0000, v13
	v_mul_f32_e32 v13, v35, v13
	v_fmac_f32_e32 v13, v34, v11
	v_add_f32_e32 v11, v12, v13
	v_and_b32_e32 v13, 0xffff0000, v14
	v_lshlrev_b32_e32 v12, 16, v14
	v_mul_f32_e32 v13, v29, v13
	v_fmac_f32_e32 v13, v28, v12
	v_add_f32_e32 v11, v13, v11
	v_and_b32_e32 v13, 0xffff0000, v15
	v_lshlrev_b32_e32 v12, 16, v15
	v_mul_f32_e32 v13, v31, v13
	v_add_f32_e32 v10, v16, v10
	v_fmac_f32_e32 v13, v30, v12
	v_add_f32_e32 v10, v20, v10
	v_add_f32_e32 v11, v13, v11
	v_add_f32_e32 v28, v10, v11
	global_load_dwordx4 v[10:13], v22, s[8:9] offset:240
	global_load_dwordx4 v[14:17], v22, s[8:9] offset:224
	global_load_dwordx4 v[18:21], v22, s[8:9] offset:208
	s_nop 0
	global_load_dwordx4 v[22:25], v22, s[8:9] offset:192
	v_lshlrev_b32_e32 v29, 16, v6
	v_and_b32_e32 v6, 0xffff0000, v6
	s_waitcnt vmcnt(0)
	v_mul_f32_e32 v6, v23, v6
	v_fmac_f32_e32 v6, v22, v29
	v_lshlrev_b32_e32 v22, 16, v7
	v_and_b32_e32 v7, 0xffff0000, v7
	v_mul_f32_e32 v7, v25, v7
	v_fmac_f32_e32 v7, v24, v22
	v_add_f32_e32 v6, v6, v7
	v_lshlrev_b32_e32 v7, 16, v8
	v_and_b32_e32 v8, 0xffff0000, v8
	v_mul_f32_e32 v8, v19, v8
	v_fmac_f32_e32 v8, v18, v7
	v_add_f32_e32 v6, v8, v6
	v_and_b32_e32 v8, 0xffff0000, v9
	v_lshlrev_b32_e32 v7, 16, v9
	v_mul_f32_e32 v8, v21, v8
	v_fmac_f32_e32 v8, v20, v7
	v_lshlrev_b32_e32 v7, 16, v2
	v_and_b32_e32 v2, 0xffff0000, v2
	v_mul_f32_e32 v2, v15, v2
	v_fmac_f32_e32 v2, v14, v7
	v_lshlrev_b32_e32 v7, 16, v3
	v_and_b32_e32 v3, 0xffff0000, v3
	v_mul_f32_e32 v3, v17, v3
	v_fmac_f32_e32 v3, v16, v7
	v_add_f32_e32 v2, v2, v3
	v_lshlrev_b32_e32 v3, 16, v4
	v_and_b32_e32 v4, 0xffff0000, v4
	v_mul_f32_e32 v4, v11, v4
	v_fmac_f32_e32 v4, v10, v3
	v_add_f32_e32 v2, v4, v2
	v_and_b32_e32 v4, 0xffff0000, v5
	v_lshlrev_b32_e32 v3, 16, v5
	v_mul_f32_e32 v4, v13, v4
	v_add_f32_e32 v6, v8, v6
	v_fmac_f32_e32 v4, v12, v3
	v_add_f32_e32 v6, v28, v6
	v_add_f32_e32 v2, v4, v2
	v_cndmask_b32_e32 v3, v212, v220, vcc
	v_add_f32_e32 v2, v6, v2
	v_lshlrev_b32_e32 v3, 2, v3
	ds_bpermute_b32 v3, v3, v2
	s_waitcnt lgkmcnt(0)
	v_add_f32_e32 v2, v2, v3
	v_xor_b32_e32 v3, 2, v212
	v_cmp_lt_i32_e32 vcc, v3, v213
	s_nop 1
	v_cndmask_b32_e32 v3, v212, v3, vcc
	v_lshlrev_b32_e32 v3, 2, v3
	ds_bpermute_b32 v3, v3, v2
	s_waitcnt lgkmcnt(0)
	v_add_f32_e32 v2, v2, v3
	v_xor_b32_e32 v3, 4, v212
	v_cmp_lt_i32_e32 vcc, v3, v213
	s_nop 1
	v_cndmask_b32_e32 v3, v212, v3, vcc
	v_lshlrev_b32_e32 v3, 2, v3
	ds_bpermute_b32 v3, v3, v2
	s_waitcnt lgkmcnt(0)
	v_add_f32_e32 v2, v2, v3
	v_xor_b32_e32 v3, 8, v212
	v_cmp_lt_i32_e32 vcc, v3, v213
	s_nop 1
	v_cndmask_b32_e32 v3, v212, v3, vcc
	v_lshlrev_b32_e32 v3, 2, v3
	ds_bpermute_b32 v3, v3, v2
	v_cmp_lt_i32_e32 vcc, v216, v213
	s_waitcnt lgkmcnt(0)
	v_add_f32_e32 v2, v2, v3
	v_cndmask_b32_e32 v3, v212, v216, vcc
	v_lshlrev_b32_e32 v3, 2, v3
	ds_bpermute_b32 v3, v3, v2
	v_cmp_eq_u32_e32 vcc, 0, v1
	s_and_saveexec_b64 s[12:13], vcc
	s_cbranch_execz .LBB0_778
	v_readlane_b32 s8, v252, 20
	v_readlane_b32 s9, v252, 21
	s_waitcnt lgkmcnt(0)
	v_add_f32_e32 v1, v2, v3
	v_lshl_add_u64 v[4:5], v[26:27], 2, s[8:9]
	global_store_dword v[4:5], v1, off

; #define PW_SYNC do { asm volatile("s_waitcnt lgkmcnt(0)" ::: "memory"); __builtin_amdgcn_s_barrier(); asm volatile("" ::: "memory"); } while (0)
; __device__ __forceinline__ void ph_weights(const Params& p, LAS unsigned char* lds, const int p0, const int p1, const int wi, const int wn) {
;     ...
;     int pi = p0 + wi; bool hA, hB;
;     PW_LOAD(pi, dA0, dA1, a0, a1, hA);
;     PW_LOAD(pi + wn, dB0, dB1, b0, b1, hB);
;     while (hA) {
;         { PW_TOLDS(dA0, a0, a1); PW_SYNC; const TDesc s0 = dA0, s1 = dA1; PW_LOAD(pi + 2 * wn, dA0, dA1, a0, a1, hA); PW_STORE(s0, s1); PW_SYNC; }
;         if (!hB) break;
;         { PW_TOLDS(dB0, b0, b1); PW_SYNC; const TDesc s0 = dB0, s1 = dB1; PW_LOAD(pi + 3 * wn, dB0, dB1, b0, b1, hB); PW_STORE(s0, s1); PW_SYNC; }
;         pi += 2 * wn;
;     }
; __global__ void __launch_bounds__(512, 2) mk_fwd(Params p) {
;     ...
;             } else { if (bx - MIX_GW < 4) ph_rbias(p, 0, bx - MIX_GW); ph_weights(p, lds, 240, 6880, bx - MIX_GW, G - MIX_GW); }
.LBB0_779:
	v_readlane_b32 s0, v249, 28
	s_nop 3
	s_cmpk_lt_u32 s0, 0xa0
	s_cbranch_scc1 .Lcv_late
	s_mul_i32 s0, s0, 2
	s_add_u32 s0, s0, 4294967216
	s_movk_i32 s70, 190
	s_movk_i32 s73, 2
	s_movk_i32 s71, 0x16b0
	s_mov_b32 s74, 0
	v_writelane_b32 v255, s29, 61
	s_branch .Lcv_common
